# P0: workgroups that ran an S5 unit (the prologue's long pole) no longer issue the (always empty by then) transpose-queue claim; the other 192 workgroups drain the queue
# speedup vs baseline: 1.0054x; 1.0054x over previous
; #define LAS __attribute__((address_space(3)))
; DI kptr_t kargs_now() { kptr_t p = (kptr_t)__builtin_amdgcn_kernarg_segment_ptr(); asm volatile("" : "+s"(p)); return p; }
; #define RI_NEXT(D_) do { if (q.cnt == 8) { int b_ = 0; if (F.lane == 0) b_ = (int)__hip_atomic_fetch_add(qctr, 8u, __ATOMIC_RELAXED, __HIP_MEMORY_SCOPE_AGENT); q.base = __builtin_amdgcn_readfirstlane(b_); q.cnt = 0; } \
;         D_ = decode_item(KA, F.ws, kind, q.base + q.cnt); ++q.cnt; } while (0)
; DI void run_items1(Frame& F, int kind, int quota, QState& q) {
;     const kptr_t KA = kargs_now();
;     LAS float* scr = (LAS float*)(F.lds + F.wave * 16384);
;     unsigned* qctr = F.ctl + CW_QUEUE + 64 * kind;
;     ...
;     if (quota == 0) return;
;     TItem d; RI_NEXT(d); if (!d.valid) return;
.LBB0_79:
	s_mov_b32 s2, -1
	s_add_u32 s0, s46, 0x8000
	v_mbcnt_lo_u32_b32 v1, s2, 0
	v_mbcnt_hi_u32_b32 v64, s2, v1
	s_mov_b32 s2, s88
	s_addc_u32 s1, s47, 0
	v_mov_b32_e32 v0, 0
	s_mov_b64 s[2:3], s[70:71]
	v_cmp_eq_u32_e64 s[4:5], 0, v64
	v_readlane_b32 s8, v253, 29
	v_readlane_b32 s9, v253, 25
	s_cmp_lt_u32 s8, 64
	s_cselect_b32 s8, 1, 0
	s_cmpk_eq_u32 s9, 0x100
	s_cselect_b32 s9, 1, 0
	s_mov_b64 s[6:7], exec
	v_mov_b32_e32 v0, 0xd00
	s_and_b32 s8, s8, s9
	s_cbranch_scc1 .LBB0_83
	v_mov_b32_e32 v0, 0
	s_and_saveexec_b64 s[6:7], s[4:5]
	s_cbranch_execz .LBB0_83
	s_mov_b64 s[10:11], exec
	v_mbcnt_lo_u32_b32 v0, s10, 0
	v_mbcnt_hi_u32_b32 v0, s11, v0
	v_cmp_eq_u32_e32 vcc, 0, v0
	s_and_saveexec_b64 s[8:9], vcc
	s_cbranch_execz .LBB0_82
	s_bcnt1_i32_b64 s10, s[10:11]
	s_lshl_b32 s10, s10, 1
	v_mov_b32_e32 v1, 0
	v_mov_b32_e32 v2, s10
	global_atomic_add v1, v1, v2, s[0:1] sc0
